# baseline (speedup 1.0000x reference)
.LBB1_6:
	v_and_b32_e32 v1, 31, v0
	v_lshl_or_b32 v2, s10, 5, v1
	v_ashrrev_i32_e32 v3, 31, v2
	s_waitcnt lgkmcnt(0)
	v_lshl_add_u64 v[2:3], v[2:3], 2, s[4:5]
	global_load_dword v104, v[2:3], off
	s_mov_b32 s11, 0
	v_lshrrev_b32_e32 v2, 2, v0
	v_and_b32_e32 v1, 15, v0
	s_lshl_b32 s5, s10, 6
	v_and_b32_e32 v2, 48, v2
	s_and_b32 s3, s2, 31
	v_or3_b32 v86, s5, v2, v1
	s_lshl_b32 s10, s3, 11
	v_ashrrev_i32_e32 v87, 31, v86
	v_lshl_add_u64 v[2:3], v[86:87], 0, s[10:11]
	v_lshlrev_b64 v[2:3], 7, v[2:3]
	v_lshl_add_u64 v[2:3], s[12:13], 0, v[2:3]
	v_mov_b32_e32 v5, 0
	v_and_b32_e32 v4, 48, v0
	v_lshl_add_u64 v[10:11], v[2:3], 0, v[4:5]
	global_load_dwordx4 v[2:5], v[10:11], off
	global_load_dwordx4 v[6:9], v[10:11], off offset:64
	v_bfe_u32 v10, v0, 4, 2
	v_and_b32_e32 v11, 63, v0
	v_lshlrev_b32_e32 v88, 3, v10
	s_lshl_b32 s1, s10, 7
	v_lshrrev_b32_e32 v13, 3, v0
	s_add_u32 s12, s14, s1
	v_mov_b32_e32 v12, 0
	v_lshlrev_b32_e32 v32, 7, v13
	s_addc_u32 s13, s15, 0
	s_mov_b64 s[84:85], s[12:13]
	v_mov_b32_e32 v33, v12
	v_lshl_add_u64 v[14:15], s[12:13], 0, v[32:33]
	s_add_u32 s12, s16, s1
	v_lshlrev_b32_e32 v90, 4, v0
	s_addc_u32 s13, s17, 0
	s_mov_b64 s[86:87], s[12:13]
	v_mov_b32_e32 v91, v12
	v_lshl_add_u64 v[94:95], s[12:13], 0, v[90:91]
	v_and_b32_e32 v16, 0x70, v90
	v_mov_b32_e32 v17, v12
	v_lshl_add_u64 v[92:93], v[14:15], 0, v[16:17]
	v_lshl_add_u64 v[96:97], v[86:87], 3, s[18:19]
	s_mov_b64 s[88:89], s[18:19]
	v_lshlrev_b32_e32 v118, 3, v86
	v_add_u32_e32 v119, 0x1000, v90
	s_mov_b32 s0, 0
	s_lshl_b32 s12, s0, 6
	s_ashr_i32 s1, s0, 31
	s_lshl_b64 s[14:15], s[0:1], 13
	s_ashr_i32 s13, s12, 31
	v_lshl_add_u64 v[26:27], v[94:95], 0, s[14:15]
	s_lshl_b64 s[14:15], s[12:13], 7
	s_or_b32 s12, s12, 32
	s_movk_i32 s5, 0x1000
	global_load_dwordx4 v[14:17], v[26:27], off
	s_ashr_i32 s13, s12, 31
	v_add_co_u32_e32 v26, vcc, s5, v26
	v_lshl_add_u64 v[28:29], v[92:93], 0, s[14:15]
	s_lshl_b64 s[12:13], s[12:13], 7
	v_addc_co_u32_e32 v27, vcc, 0, v27, vcc
	v_lshl_add_u64 v[30:31], v[92:93], 0, s[12:13]
	global_load_dwordx4 v[22:25], v[28:29], off
	global_load_dwordx4 v[18:21], v[30:31], off
	global_load_dwordx4 v[26:29], v[26:27], off
	s_lshl_b64 s[12:13], s[0:1], 14
	v_lshl_add_u64 v[30:31], v[96:97], 0, s[12:13]
	global_load_dwordx2 v[102:103], v[30:31], off
	s_waitcnt vmcnt(7)
	v_cmp_ne_u32_e64 s[8:9], 0, v104
	v_cmp_eq_u32_e64 s[6:7], 2, v104
	s_cmp_eq_u32 s8, 0
	v_cmp_eq_u32_e64 s[4:5], 3, v104
	s_cbranch_scc1 .LBB1_48
	s_branch .LBB1_10

.LBB1_25:
	s_cmp_gt_i32 s16, -1
	s_cselect_b64 s[18:19], -1, 0
	s_cmp_lt_i32 s16, 0
	s_cbranch_scc1 .LBB1_27
	s_lshl_b32 s22, s16, 13
	s_add_u32 s24, s86, s22
	s_addc_u32 s25, s87, 0
	s_add_u32 s26, s84, s22
	s_addc_u32 s27, s85, 0
	s_lshl_b32 s22, s16, 14
	s_add_u32 s28, s88, s22
	s_addc_u32 s29, s89, 0
	global_load_dwordx4 v[14:17], v90, s[24:25]
	global_load_dwordx4 v[22:25], v90, s[26:27]
	global_load_dwordx4 v[18:21], v119, s[26:27]
	global_load_dwordx4 v[26:29], v119, s[24:25]
	global_load_dwordx2 v[100:101], v118, s[28:29]

	.amdhsa_kernel _Z11attn_kernelPKDF16_S0_S0_PKyPKiPDF16_
		.amdhsa_group_segment_fixed_size 36864
		.amdhsa_private_segment_fixed_size 0
		.amdhsa_kernarg_size 48
		.amdhsa_user_sgpr_count 2
		.amdhsa_user_sgpr_dispatch_ptr 0
		.amdhsa_user_sgpr_queue_ptr 0
		.amdhsa_user_sgpr_kernarg_segment_ptr 1
		.amdhsa_user_sgpr_dispatch_id 0
		.amdhsa_user_sgpr_kernarg_preload_length 0
		.amdhsa_user_sgpr_kernarg_preload_offset 0
		.amdhsa_user_sgpr_private_segment_size 0
		.amdhsa_uses_dynamic_stack 0
		.amdhsa_enable_private_segment 0
		.amdhsa_system_sgpr_workgroup_id_x 1
		.amdhsa_system_sgpr_workgroup_id_y 0
		.amdhsa_system_sgpr_workgroup_id_z 0
		.amdhsa_system_sgpr_workgroup_info 0
		.amdhsa_system_vgpr_workitem_id 0
		.amdhsa_next_free_vgpr 120
		.amdhsa_next_free_sgpr 96
		.amdhsa_accum_offset 120
		.amdhsa_reserve_vcc 1
		.amdhsa_float_round_mode_32 0
		.amdhsa_float_round_mode_16_64 0
		.amdhsa_float_denorm_mode_32 3
		.amdhsa_float_denorm_mode_16_64 3
		.amdhsa_dx10_clamp 1
		.amdhsa_ieee_mode 1
		.amdhsa_fp16_overflow 0
		.amdhsa_tg_split 0
		.amdhsa_exception_fp_ieee_invalid_op 0
		.amdhsa_exception_fp_denorm_src 0
		.amdhsa_exception_fp_ieee_div_zero 0
		.amdhsa_exception_fp_ieee_overflow 0
		.amdhsa_exception_fp_ieee_underflow 0
		.amdhsa_exception_fp_ieee_inexact 0
		.amdhsa_exception_int_div_zero 0
	.end_amdhsa_kernel

amdhsa.kernels:
  - .agpr_count:     0
    .args:
      - .actual_access:  read_only
        .address_space:  global
        .offset:         0
        .size:           8
        .value_kind:     global_buffer
      - .actual_access:  read_only
        .address_space:  global
        .offset:         8
        .size:           8
        .value_kind:     global_buffer
      - .actual_access:  read_only
        .address_space:  global
        .offset:         16
        .size:           8
        .value_kind:     global_buffer
      - .actual_access:  read_only
        .address_space:  global
        .offset:         24
        .size:           8
        .value_kind:     global_buffer
      - .actual_access:  read_only
        .address_space:  global
        .offset:         32
        .size:           8
        .value_kind:     global_buffer
      - .actual_access:  read_only
        .address_space:  global
        .offset:         40
        .size:           8
        .value_kind:     global_buffer
      - .actual_access:  write_only
        .address_space:  global
        .offset:         48
        .size:           8
        .value_kind:     global_buffer
      - .actual_access:  write_only
        .address_space:  global
        .offset:         56
        .size:           8
        .value_kind:     global_buffer
      - .actual_access:  write_only
        .address_space:  global
        .offset:         64
        .size:           8
        .value_kind:     global_buffer
      - .actual_access:  write_only
        .address_space:  global
        .offset:         72
        .size:           8
        .value_kind:     global_buffer
      - .actual_access:  write_only
        .address_space:  global
        .offset:         80
        .size:           8
        .value_kind:     global_buffer
    .group_segment_fixed_size: 16640
    .kernarg_segment_align: 8
    .kernarg_segment_size: 88
    .language:       OpenCL C
    .language_version:
      - 2
      - 0
    .max_flat_workgroup_size: 256
    .name:           _Z11prep_kernelPKfS0_S0_S0_S0_PKiPDF16_S3_S3_PyPi
    .private_segment_fixed_size: 0
    .sgpr_count:     54
    .sgpr_spill_count: 0
    .symbol:         _Z11prep_kernelPKfS0_S0_S0_S0_PKiPDF16_S3_S3_PyPi.kd
    .uniform_work_group_size: 1
    .uses_dynamic_stack: false
    .vgpr_count:     46
    .vgpr_spill_count: 0
    .wavefront_size: 64
  - .agpr_count:     0
    .args:
      - .actual_access:  read_only
        .address_space:  global
        .offset:         0
        .size:           8
        .value_kind:     global_buffer
      - .actual_access:  read_only
        .address_space:  global
        .offset:         8
        .size:           8
        .value_kind:     global_buffer
      - .actual_access:  read_only
        .address_space:  global
        .offset:         16
        .size:           8
        .value_kind:     global_buffer
      - .actual_access:  read_only
        .address_space:  global
        .offset:         24
        .size:           8
        .value_kind:     global_buffer
      - .actual_access:  read_only
        .address_space:  global
        .offset:         32
        .size:           8
        .value_kind:     global_buffer
      - .actual_access:  write_only
        .address_space:  global
        .offset:         40
        .size:           8
        .value_kind:     global_buffer
    .group_segment_fixed_size: 36864
    .kernarg_segment_align: 8
    .kernarg_segment_size: 48
    .language:       OpenCL C
    .language_version:
      - 2
      - 0
    .max_flat_workgroup_size: 256
    .name:           _Z11attn_kernelPKDF16_S0_S0_PKyPKiPDF16_
    .private_segment_fixed_size: 0
    .sgpr_count:     32
    .sgpr_spill_count: 0
    .symbol:         _Z11attn_kernelPKDF16_S0_S0_PKyPKiPDF16_.kd
    .uniform_work_group_size: 1
    .uses_dynamic_stack: false
    .vgpr_count:     120
    .vgpr_spill_count: 0
    .wavefront_size: 64
  - .agpr_count:     0
    .args:
      - .address_space:  global
        .offset:         0
        .size:           8
        .value_kind:     global_buffer
      - .address_space:  global
        .offset:         8
        .size:           8
        .value_kind:     global_buffer
      - .actual_access:  read_only
        .address_space:  global
        .offset:         16
        .size:           8
        .value_kind:     global_buffer
      - .actual_access:  read_only
        .address_space:  global
        .offset:         24
        .size:           8
        .value_kind:     global_buffer
      - .actual_access:  read_only
        .address_space:  global
        .offset:         32
        .size:           8
        .value_kind:     global_buffer
      - .actual_access:  read_only
        .address_space:  global
        .offset:         40
        .size:           8
        .value_kind:     global_buffer
      - .actual_access:  write_only
        .address_space:  global
        .offset:         48
        .size:           8
        .value_kind:     global_buffer
      - .actual_access:  write_only
        .address_space:  global
        .offset:         56
        .size:           8
        .value_kind:     global_buffer
      - .actual_access:  write_only
        .address_space:  global
        .offset:         64
        .size:           8
        .value_kind:     global_buffer
    .group_segment_fixed_size: 114688
    .kernarg_segment_align: 8
    .kernarg_segment_size: 72
    .language:       OpenCL C
    .language_version:
      - 2
      - 0
    .max_flat_workgroup_size: 512
    .name:           _Z9gemm_gldsILi256ELi192ELi4ELi2ELi2ELi4ELi8ELi0ELi4096ELi3072ELi1024EEvPKDF16_S1_PfPKfS4_PKiPDF16_S7_S7_
    .private_segment_fixed_size: 0
    .sgpr_count:     29
    .sgpr_spill_count: 0
    .symbol:         _Z9gemm_gldsILi256ELi192ELi4ELi2ELi2ELi4ELi8ELi0ELi4096ELi3072ELi1024EEvPKDF16_S1_PfPKfS4_PKiPDF16_S7_S7_.kd
    .uniform_work_group_size: 1
    .uses_dynamic_stack: false
    .vgpr_count:     214
    .vgpr_spill_count: 0
    .wavefront_size: 64
  - .agpr_count:     0
    .args:
      - .address_space:  global
        .offset:         0
        .size:           8
        .value_kind:     global_buffer
      - .address_space:  global
        .offset:         8
        .size:           8
        .value_kind:     global_buffer
      - .actual_access:  write_only
        .address_space:  global
        .offset:         16
        .size:           8
        .value_kind:     global_buffer
      - .actual_access:  read_only
        .address_space:  global
        .offset:         24
        .size:           8
        .value_kind:     global_buffer
      - .actual_access:  read_only
        .address_space:  global
        .offset:         32
        .size:           8
        .value_kind:     global_buffer
      - .actual_access:  read_only
        .address_space:  global
        .offset:         40
        .size:           8
        .value_kind:     global_buffer
      - .actual_access:  read_only
        .address_space:  global
        .offset:         48
        .size:           8
        .value_kind:     global_buffer
      - .actual_access:  read_only
        .address_space:  global
        .offset:         56
        .size:           8
        .value_kind:     global_buffer
      - .actual_access:  read_only
        .address_space:  global
        .offset:         64
        .size:           8
        .value_kind:     global_buffer
    .group_segment_fixed_size: 98304
    .kernarg_segment_align: 8
    .kernarg_segment_size: 72
    .language:       OpenCL C
    .language_version:
      - 2
      - 0
    .max_flat_workgroup_size: 512
    .name:           _Z9gemm_gldsILi128ELi128ELi4ELi2ELi3ELi8ELi4ELi1ELi4096ELi1024ELi1024EEvPKDF16_S1_PfPKfS4_PKiPDF16_S7_S7_
    .private_segment_fixed_size: 0
    .sgpr_count:     20
    .sgpr_spill_count: 0
    .symbol:         _Z9gemm_gldsILi128ELi128ELi4ELi2ELi3ELi8ELi4ELi1ELi4096ELi1024ELi1024EEvPKDF16_S1_PfPKfS4_PKiPDF16_S7_S7_.kd
    .uniform_work_group_size: 1
    .uses_dynamic_stack: false
    .vgpr_count:     92
    .vgpr_spill_count: 0
    .wavefront_size: 64
